# v048 + one deferred conversion item per wave also hosted by the 248 workgroups idle during the ctx out-projection call (P4b)
# speedup vs baseline: 1.0236x; 1.0031x over previous
; #define LAS __attribute__((address_space(3)))
; __device__ __forceinline__ int tidx() { int t = threadIdx.x; asm volatile("" : "+v"(t)); return t; }
; __device__ __forceinline__ void phase_cvt_moe(LAS unsigned char* lds, const CvtMoe a) {
;     const int tid_ = tidx(), wave = tid_ >> 6, lane = tid_ & 63;
;     LAS float* scr = (LAS float*)(lds + wave * CVT_SCR);
;     const int gw = blockIdx.x * 8 + wave, NGW = gridDim.x * 8;
;     constexpr int IG = (D / 64) * (FF / 64), ID = (FF / 64) * (D / 64);
;     for (int it = gw; it < 2 * NE * (2 * IG + ID); it += NGW) {
;         const int e = it / (2 * IG + ID); int r = it % (2 * IG + ID);
;         if (r < 2 * IG) { const int up = r / IG; r %= IG; const int nblk = FF / 64, kb = r / nblk, nb = r % nblk, n0 = nb * 64;
.LBB0_55:
	s_or_b64 exec, exec, s[4:5]
	s_add_u32 s4, s90, 0x30a13600
	s_addc_u32 s5, s91, 0
	v_writelane_b32 v250, s4, 6
	v_mov_b32_e32 v4, v0
	s_nop 0
	v_writelane_b32 v250, s5, 7
	s_add_u32 s4, s90, 0x46a13600
	s_addc_u32 s5, s91, 0
	v_writelane_b32 v250, s4, 8
	v_ashrrev_i32_e32 v2, 6, v4
	v_add_u32_e32 v5, s14, v2
	v_writelane_b32 v250, s5, 9
	s_mov_b32 s4, 0xd940
	v_cmp_gt_i32_e32 vcc, s4, v5
	s_and_saveexec_b64 s[4:5], vcc
	s_cbranch_execz .LBB0_62
	s_movk_i32 s6, 0x4100
	v_mul_lo_u32 v3, v2, s6
	v_add_u32_e32 v8, 0, v3
	v_lshlrev_b32_e32 v3, 2, v4
	v_bfe_u32 v6, v4, 4, 2
	v_and_b32_e32 v44, 60, v3
	v_bfe_u32 v7, v4, 3, 3
	v_lshlrev_b32_e32 v4, 3, v4
	v_lshl_add_u32 v20, v44, 2, v8
	v_mul_u32_u24_e32 v21, 0x104, v6
	v_and_b32_e32 v4, 56, v4
	v_mul_u32_u24_e32 v9, 0x104, v4
	v_lshlrev_b32_e32 v10, 2, v7
	v_lshlrev_b32_e32 v16, 2, v2
	v_add_u32_e32 v20, v20, v21
	v_mov_b32_e32 v3, 0
	v_add3_u32 v8, v8, v9, v10
	v_or_b32_e32 v9, 8, v7
	v_or_b32_e32 v10, 16, v7
	v_or_b32_e32 v11, 24, v7
	v_or_b32_e32 v12, 32, v7
	v_or_b32_e32 v13, 40, v7
	v_or_b32_e32 v14, 48, v7
	v_or_b32_e32 v15, 56, v7
	v_lshl_add_u32 v16, s2, 5, v16
	v_lshlrev_b32_e32 v17, 2, v1
	v_lshl_add_u32 v18, v2, 6, s3
	v_lshlrev_b32_e32 v19, 6, v1
	s_mov_b64 s[6:7], 0
	s_mov_b32 s3, 0x3e0f83e1
	s_movk_i32 s10, 0x57f
	s_mov_b32 s11, 0xb00000
	v_add_u32_e32 v21, 0x410, v20
	v_add_u32_e32 v22, 0x418, v20
	v_add_u32_e32 v23, 0x820, v20
	v_add_u32_e32 v24, 0x828, v20
	v_add_u32_e32 v25, 0xc30, v20
	v_add_u32_e32 v26, 0xc38, v20
	v_add_u32_e32 v27, 0x1040, v20
	v_add_u32_e32 v28, 0x1048, v20
	v_add_u32_e32 v29, 0x1450, v20
	v_add_u32_e32 v30, 0x1458, v20
	v_add_u32_e32 v31, 0x1860, v20
	v_add_u32_e32 v32, 0x1868, v20
	v_add_u32_e32 v33, 0x1c70, v20
	v_add_u32_e32 v34, 0x1c78, v20
	v_add_u32_e32 v35, 0x2080, v20
	v_add_u32_e32 v36, 0x2088, v20
	v_add_u32_e32 v37, 0x2490, v20
	v_add_u32_e32 v38, 0x2498, v20
	v_add_u32_e32 v39, 0x28a0, v20
	v_add_u32_e32 v40, 0x28a8, v20
	v_add_u32_e32 v41, 0x2cb0, v20
	v_add_u32_e32 v42, 0x2cb8, v20
	s_movk_i32 s12, 0xba3
	s_mov_b32 s13, 0xb000
	s_mov_b32 s14, 0x16000
	s_mov_b32 s15, 0x21000
	s_mov_b32 s16, 0x2c000
	s_mov_b32 s17, 0x37000
	s_mov_b32 s18, 0x42000
	s_mov_b32 s19, 0x4d000
	s_mov_b32 s20, 0x58000
	s_mov_b32 s21, 0x63000
	s_mov_b32 s22, 0x6e000
	s_mov_b32 s23, 0x79000
	s_mov_b32 s24, 0x84000
	s_mov_b32 s25, 0x8f000
	s_mov_b32 s26, 0x9a000
	s_mov_b32 s27, 0xa5000
	s_mov_b32 s28, 0xd93f
	v_lshlrev_b32_e32 v2, 2, v44
	v_add_u32_e32 v43, 0x30c0, v20
	v_add_u32_e32 v44, 0x30c8, v20
	v_add_u32_e32 v45, 0x34d0, v20
	v_add_u32_e32 v46, 0x34d8, v20
	v_mov_b32_e32 v47, 6
	v_mov_b32_e32 v48, 1
	v_mov_b32_e32 v49, 8
	v_mov_b32_e32 v50, 7
	s_branch .LBB0_58

; #define LAS __attribute__((address_space(3)))
; __device__ __forceinline__ int tidx() { int t = threadIdx.x; asm volatile("" : "+v"(t)); return t; }
; __device__ __forceinline__ void phase_cvt_moe(LAS unsigned char* lds, const CvtMoe a) {
;     const int tid_ = tidx(), wave = tid_ >> 6, lane = tid_ & 63;
;     LAS float* scr = (LAS float*)(lds + wave * CVT_SCR);
;     const int gw = blockIdx.x * 8 + wave, NGW = gridDim.x * 8;
;     constexpr int IG = (D / 64) * (FF / 64), ID = (FF / 64) * (D / 64);
;     for (int it = gw; it < 2 * NE * (2 * IG + ID); it += NGW) {
;         const int e = it / (2 * IG + ID); int r = it % (2 * IG + ID);
;         if (r < 2 * IG) { const int up = r / IG; r %= IG; const int nblk = FF / 64, kb = r / nblk, nb = r % nblk, n0 = nb * 64;
.Lcvp4b_entry:
	s_sub_i32 s0, s94, 8
	v_readlane_b32 s2, v250, 26
	v_readlane_b32 s3, v250, 27
	s_nop 3
	s_sub_u32 s2, s2, 0xc0
	s_subb_u32 s3, s3, 0
	s_load_dwordx2 s[38:39], s[2:3], 0x90
	s_load_dwordx2 s[40:41], s[2:3], 0x98
	s_load_dwordx2 s[34:35], s[2:3], 0xa0
	s_lshl_b32 s0, s0, 3
	s_add_i32 s0, s0, 0xd940
	v_mov_b32_e32 v131, 0x7c0
	s_waitcnt lgkmcnt(0)
	s_add_u32 s4, s90, 0x30a13600
	s_addc_u32 s5, s91, 0
	v_writelane_b32 v250, s4, 6
	v_mov_b32_e32 v130, v0
	s_nop 0
	v_writelane_b32 v250, s5, 7
	s_add_u32 s4, s90, 0x46a13600
	s_addc_u32 s5, s91, 0
	v_writelane_b32 v250, s4, 8
	v_ashrrev_i32_e32 v2, 6, v130
	v_add_u32_e32 v5, s0, v2
	v_writelane_b32 v250, s5, 9
	s_mov_b32 s4, 0xe100
	v_cmp_gt_i32_e32 vcc, s4, v5
	s_and_saveexec_b64 s[4:5], vcc
	s_cbranch_execz .Lcvp4b_62
	s_movk_i32 s6, 0x4100
	v_mul_lo_u32 v3, v2, s6
	v_add_u32_e32 v8, 0, v3
	v_lshlrev_b32_e32 v3, 2, v130
	v_bfe_u32 v6, v130, 4, 2
	v_and_b32_e32 v44, 60, v3
	v_bfe_u32 v7, v130, 3, 3
	v_lshlrev_b32_e32 v130, 3, v130
	v_lshl_add_u32 v20, v44, 2, v8
	v_mul_u32_u24_e32 v21, 0x104, v6
	v_and_b32_e32 v130, 56, v130
	v_mul_u32_u24_e32 v9, 0x104, v130
	v_lshlrev_b32_e32 v10, 2, v7
	v_lshlrev_b32_e32 v16, 2, v2
	v_add_u32_e32 v20, v20, v21
	v_mov_b32_e32 v3, 0
	v_add3_u32 v8, v8, v9, v10
	v_or_b32_e32 v9, 8, v7
	v_or_b32_e32 v10, 16, v7
	v_or_b32_e32 v11, 24, v7
	v_or_b32_e32 v12, 32, v7
	v_or_b32_e32 v13, 40, v7
	v_or_b32_e32 v14, 48, v7
	v_or_b32_e32 v15, 56, v7
	v_lshlrev_b32_e32 v16, 2, v5
	v_lshlrev_b32_e32 v17, 2, v131
	v_lshlrev_b32_e32 v18, 6, v5
	v_lshlrev_b32_e32 v19, 6, v131
	s_mov_b64 s[6:7], 0
	s_mov_b32 s3, 0x3e0f83e1
	s_movk_i32 s10, 0x57f
	s_mov_b32 s11, 0xb00000
	v_add_u32_e32 v21, 0x410, v20
	v_add_u32_e32 v22, 0x418, v20
	v_add_u32_e32 v23, 0x820, v20
	v_add_u32_e32 v24, 0x828, v20
	v_add_u32_e32 v25, 0xc30, v20
	v_add_u32_e32 v26, 0xc38, v20
	v_add_u32_e32 v27, 0x1040, v20
	v_add_u32_e32 v28, 0x1048, v20
	v_add_u32_e32 v29, 0x1450, v20
	v_add_u32_e32 v30, 0x1458, v20
	v_add_u32_e32 v31, 0x1860, v20
	v_add_u32_e32 v32, 0x1868, v20
	v_add_u32_e32 v33, 0x1c70, v20
	v_add_u32_e32 v34, 0x1c78, v20
	v_add_u32_e32 v35, 0x2080, v20
	v_add_u32_e32 v36, 0x2088, v20
	v_add_u32_e32 v37, 0x2490, v20
	v_add_u32_e32 v38, 0x2498, v20
	v_add_u32_e32 v39, 0x28a0, v20
	v_add_u32_e32 v40, 0x28a8, v20
	v_add_u32_e32 v41, 0x2cb0, v20
	v_add_u32_e32 v42, 0x2cb8, v20
	s_movk_i32 s64, 0xba3
	s_mov_b32 s65, 0xb000
	s_mov_b32 s66, 0x16000
	s_mov_b32 s67, 0x21000
	s_mov_b32 s16, 0x2c000
	s_mov_b32 s68, 0x37000
	s_mov_b32 s69, 0x42000
	s_mov_b32 s19, 0x4d000
	s_mov_b32 s20, 0x58000
	s_mov_b32 s21, 0x63000
	s_mov_b32 s70, 0x6e000
	s_mov_b32 s23, 0x79000
	s_mov_b32 s24, 0x84000
	s_mov_b32 s25, 0x8f000
	s_mov_b32 s26, 0x9a000
	s_mov_b32 s27, 0xa5000
	s_mov_b32 s71, 0xe0ff
	v_lshlrev_b32_e32 v2, 2, v44
	v_add_u32_e32 v43, 0x30c0, v20
	v_add_u32_e32 v44, 0x30c8, v20
	v_add_u32_e32 v45, 0x34d0, v20
	v_add_u32_e32 v46, 0x34d8, v20
	v_mov_b32_e32 v47, 6
	v_mov_b32_e32 v132, 1
	v_mov_b32_e32 v133, 8
	v_mov_b32_e32 v134, 7
	s_branch .Lcvp4b_58
